# P6 K-loop DMA also in scalar-base form (one saved SGPR pair + recompute of the intact base)
# baseline (speedup 1.0000x reference)
.LBB0_495:
	ds_read_b128 v[2:5], v187
	ds_read_b128 v[6:9], v187 offset:1024
	ds_read_b128 v[10:13], v187 offset:2048
	ds_read_b128 v[14:17], v187 offset:3072
	s_add_u32 s28, s26, 0xfffc0080
	s_addc_u32 s29, s27, -1
	s_cmp_eq_u32 s52, 12
	s_cselect_b32 s31, s6, s29
	s_cselect_b32 s30, s17, s28
	s_cselect_b32 s29, s15, s51
	s_cselect_b32 s28, s49, s50
	s_add_i32 m0, s37, 0xc000
	ds_read_b128 v[192:195], v188
	ds_read_b128 v[196:199], v188 offset:1024
	ds_read_b128 v[206:209], v188 offset:2048
	ds_read_b128 v[210:213], v188 offset:3072
	ds_read_b128 v[214:217], v188 offset:4096
	ds_read_b128 v[218:221], v188 offset:5120
	ds_read_b128 v[222:225], v188 offset:6144
	ds_read_b128 v[226:229], v188 offset:7168
	global_load_lds_dwordx4 v170, s[26:27]
	s_add_i32 m0, s37, 0xe000
	s_nop 0
	global_load_lds_dwordx4 v172, s[26:27]
	s_waitcnt lgkmcnt(8)
	s_barrier
	s_waitcnt lgkmcnt(0)
	s_setprio 1
	s_waitcnt lgkmcnt(0)
	v_mfma_scale_f32_16x16x128_f8f6f4 v[142:145], v[2:9], v[192:199], v[142:145], v189, v189 op_sel_hi:[0,0,0]
	v_mfma_scale_f32_16x16x128_f8f6f4 v[138:141], v[10:17], v[192:199], v[138:141], v189, v189 op_sel_hi:[0,0,0]
	v_mfma_scale_f32_16x16x128_f8f6f4 v[126:129], v[2:9], v[206:213], v[126:129], v189, v189 op_sel_hi:[0,0,0]
	v_mfma_scale_f32_16x16x128_f8f6f4 v[122:125], v[10:17], v[206:213], v[122:125], v189, v189 op_sel_hi:[0,0,0]
	v_mfma_scale_f32_16x16x128_f8f6f4 v[110:113], v[2:9], v[214:221], v[110:113], v189, v189 op_sel_hi:[0,0,0]
	v_mfma_scale_f32_16x16x128_f8f6f4 v[106:109], v[10:17], v[214:221], v[106:109], v189, v189 op_sel_hi:[0,0,0]
	v_mfma_scale_f32_16x16x128_f8f6f4 v[94:97], v[2:9], v[222:229], v[94:97], v189, v189 op_sel_hi:[0,0,0]
	v_mfma_scale_f32_16x16x128_f8f6f4 v[90:93], v[10:17], v[222:229], v[90:93], v189, v189 op_sel_hi:[0,0,0]
	s_setprio 0
	s_barrier
	s_add_i32 s53, s46, s34
	s_mov_b32 m0, s53
	ds_read_b128 v[230:233], v190
	ds_read_b128 v[234:237], v190 offset:1024
	ds_read_b128 v[238:241], v190 offset:2048
	ds_read_b128 v[242:245], v190 offset:3072
	global_load_lds_dwordx4 v150, s[28:29]
	s_add_i32 m0, s53, 0x2000
	s_nop 0
	global_load_lds_dwordx4 v146, s[28:29]
	s_barrier
	s_waitcnt lgkmcnt(0)
	s_setprio 1
	s_waitcnt lgkmcnt(0)
	v_mfma_scale_f32_16x16x128_f8f6f4 v[134:137], v[230:237], v[192:199], v[134:137], v189, v189 op_sel_hi:[0,0,0]
	v_mfma_scale_f32_16x16x128_f8f6f4 v[130:133], v[238:245], v[192:199], v[130:133], v189, v189 op_sel_hi:[0,0,0]
	v_mfma_scale_f32_16x16x128_f8f6f4 v[118:121], v[230:237], v[206:213], v[118:121], v189, v189 op_sel_hi:[0,0,0]
	v_mfma_scale_f32_16x16x128_f8f6f4 v[114:117], v[238:245], v[206:213], v[114:117], v189, v189 op_sel_hi:[0,0,0]
	v_mfma_scale_f32_16x16x128_f8f6f4 v[102:105], v[230:237], v[214:221], v[102:105], v189, v189 op_sel_hi:[0,0,0]
	v_mfma_scale_f32_16x16x128_f8f6f4 v[98:101], v[238:245], v[214:221], v[98:101], v189, v189 op_sel_hi:[0,0,0]
	v_mfma_scale_f32_16x16x128_f8f6f4 v[86:89], v[230:237], v[222:229], v[86:89], v189, v189 op_sel_hi:[0,0,0]
	v_mfma_scale_f32_16x16x128_f8f6f4 v[82:85], v[238:245], v[222:229], v[82:85], v189, v189 op_sel_hi:[0,0,0]
	s_setprio 0
	s_mov_b32 m0, s37
	s_add_u32 s56, s30, 0x80
	s_addc_u32 s57, s31, 0
	s_barrier
	ds_read_b128 v[192:195], v188 offset:16384
	ds_read_b128 v[196:199], v188 offset:17408
	ds_read_b128 v[206:209], v188 offset:18432
	ds_read_b128 v[210:213], v188 offset:19456
	ds_read_b128 v[214:217], v188 offset:20480
	ds_read_b128 v[218:221], v188 offset:21504
	ds_read_b128 v[222:225], v188 offset:22528
	ds_read_b128 v[226:229], v188 offset:23552
	global_load_lds_dwordx4 v152, s[30:31]
	s_mov_b32 m0, s38
	s_nop 0
	global_load_lds_dwordx4 v148, s[30:31]
	s_barrier
	s_waitcnt lgkmcnt(0)
	s_setprio 1
	s_waitcnt lgkmcnt(0)
	v_mfma_scale_f32_16x16x128_f8f6f4 v[78:81], v[2:9], v[192:199], v[78:81], v189, v189 op_sel_hi:[0,0,0]
	v_mfma_scale_f32_16x16x128_f8f6f4 v[74:77], v[10:17], v[192:199], v[74:77], v189, v189 op_sel_hi:[0,0,0]
	v_mfma_scale_f32_16x16x128_f8f6f4 v[62:65], v[2:9], v[206:213], v[62:65], v189, v189 op_sel_hi:[0,0,0]
	v_mfma_scale_f32_16x16x128_f8f6f4 v[58:61], v[10:17], v[206:213], v[58:61], v189, v189 op_sel_hi:[0,0,0]
	v_mfma_scale_f32_16x16x128_f8f6f4 v[46:49], v[2:9], v[214:221], v[46:49], v189, v189 op_sel_hi:[0,0,0]
	v_mfma_scale_f32_16x16x128_f8f6f4 v[42:45], v[10:17], v[214:221], v[42:45], v189, v189 op_sel_hi:[0,0,0]
	v_mfma_scale_f32_16x16x128_f8f6f4 v[30:33], v[2:9], v[222:229], v[30:33], v189, v189 op_sel_hi:[0,0,0]
	v_mfma_scale_f32_16x16x128_f8f6f4 v[26:29], v[10:17], v[222:229], v[26:29], v189, v189 op_sel_hi:[0,0,0]
	s_setprio 0
	s_barrier
	s_add_u32 s54, s28, 0x40000
	s_addc_u32 s55, s29, 0
	s_add_i32 s53, s47, s34
	s_mov_b32 m0, s53
	s_nop 0
	global_load_lds_dwordx4 v150, s[54:55]
	s_add_i32 m0, s53, 0x2000
	s_nop 0
	global_load_lds_dwordx4 v146, s[54:55]
	s_waitcnt vmcnt(6)
	s_barrier
	s_setprio 1
	v_mfma_scale_f32_16x16x128_f8f6f4 v[70:73], v[230:237], v[192:199], v[70:73], v189, v189 op_sel_hi:[0,0,0]
	v_mfma_scale_f32_16x16x128_f8f6f4 v[66:69], v[238:245], v[192:199], v[66:69], v189, v189 op_sel_hi:[0,0,0]
	v_mfma_scale_f32_16x16x128_f8f6f4 v[54:57], v[230:237], v[206:213], v[54:57], v189, v189 op_sel_hi:[0,0,0]
	v_mfma_scale_f32_16x16x128_f8f6f4 v[50:53], v[238:245], v[206:213], v[50:53], v189, v189 op_sel_hi:[0,0,0]
	v_mfma_scale_f32_16x16x128_f8f6f4 v[38:41], v[230:237], v[214:221], v[38:41], v189, v189 op_sel_hi:[0,0,0]
	v_mfma_scale_f32_16x16x128_f8f6f4 v[34:37], v[238:245], v[214:221], v[34:37], v189, v189 op_sel_hi:[0,0,0]
	v_mfma_scale_f32_16x16x128_f8f6f4 v[22:25], v[230:237], v[222:229], v[22:25], v189, v189 op_sel_hi:[0,0,0]
	v_mfma_scale_f32_16x16x128_f8f6f4 v[18:21], v[238:245], v[222:229], v[18:21], v189, v189 op_sel_hi:[0,0,0]
	s_setprio 0
	s_add_i32 s53, 0, 0x18000
	v_add_u32_e32 v14, s53, v1
	s_barrier
	ds_read_b128 v[2:5], v14
	ds_read_b128 v[6:9], v14 offset:1024
	ds_read_b128 v[10:13], v14 offset:2048
	ds_read_b128 v[14:17], v14 offset:3072
	s_add_u32 s30, s30, 0x40000
	s_addc_u32 s31, s31, 0
	s_mov_b32 m0, s39
	ds_read_b128 v[192:195], v188 offset:32768
	ds_read_b128 v[196:199], v188 offset:33792
	ds_read_b128 v[206:209], v188 offset:34816
	ds_read_b128 v[210:213], v188 offset:35840
	ds_read_b128 v[214:217], v188 offset:36864
	ds_read_b128 v[218:221], v188 offset:37888
	ds_read_b128 v[222:225], v188 offset:38912
	ds_read_b128 v[226:229], v188 offset:39936
	global_load_lds_dwordx4 v152, s[30:31]
	s_mov_b32 m0, s40
	s_nop 0
	global_load_lds_dwordx4 v148, s[30:31]
	s_waitcnt lgkmcnt(8)
	s_barrier
	s_waitcnt lgkmcnt(0)
	s_setprio 1
	s_waitcnt lgkmcnt(0)
	v_mfma_scale_f32_16x16x128_f8f6f4 v[142:145], v[2:9], v[192:199], v[142:145], v189, v189 op_sel_hi:[0,0,0]
	v_mfma_scale_f32_16x16x128_f8f6f4 v[138:141], v[10:17], v[192:199], v[138:141], v189, v189 op_sel_hi:[0,0,0]
	v_mfma_scale_f32_16x16x128_f8f6f4 v[126:129], v[2:9], v[206:213], v[126:129], v189, v189 op_sel_hi:[0,0,0]
	v_mfma_scale_f32_16x16x128_f8f6f4 v[122:125], v[10:17], v[206:213], v[122:125], v189, v189 op_sel_hi:[0,0,0]
	v_mfma_scale_f32_16x16x128_f8f6f4 v[110:113], v[2:9], v[214:221], v[110:113], v189, v189 op_sel_hi:[0,0,0]
	v_mfma_scale_f32_16x16x128_f8f6f4 v[106:109], v[10:17], v[214:221], v[106:109], v189, v189 op_sel_hi:[0,0,0]
	v_mfma_scale_f32_16x16x128_f8f6f4 v[94:97], v[2:9], v[222:229], v[94:97], v189, v189 op_sel_hi:[0,0,0]
	v_mfma_scale_f32_16x16x128_f8f6f4 v[90:93], v[10:17], v[222:229], v[90:93], v189, v189 op_sel_hi:[0,0,0]
	s_setprio 0
	s_barrier
	s_add_i32 s30, 0, 0x1c000
	s_add_i32 s31, s53, s34
	v_add_u32_e32 v191, s30, v1
	s_add_u32 s54, s28, 0x80
	s_addc_u32 s55, s29, 0
	s_mov_b32 m0, s31
	ds_read_b128 v[230:233], v191
	ds_read_b128 v[234:237], v191 offset:1024
	ds_read_b128 v[238:241], v191 offset:2048
	ds_read_b128 v[242:245], v191 offset:3072
	global_load_lds_dwordx4 v150, s[54:55]
	s_add_i32 m0, s31, 0x2000
	s_nop 0
	global_load_lds_dwordx4 v146, s[54:55]
	s_barrier
	s_waitcnt lgkmcnt(0)
	s_setprio 1
	s_waitcnt lgkmcnt(0)
	v_mfma_scale_f32_16x16x128_f8f6f4 v[134:137], v[230:237], v[192:199], v[134:137], v189, v189 op_sel_hi:[0,0,0]
	v_mfma_scale_f32_16x16x128_f8f6f4 v[130:133], v[238:245], v[192:199], v[130:133], v189, v189 op_sel_hi:[0,0,0]
	v_mfma_scale_f32_16x16x128_f8f6f4 v[118:121], v[230:237], v[206:213], v[118:121], v189, v189 op_sel_hi:[0,0,0]
	v_mfma_scale_f32_16x16x128_f8f6f4 v[114:117], v[238:245], v[206:213], v[114:117], v189, v189 op_sel_hi:[0,0,0]
	v_mfma_scale_f32_16x16x128_f8f6f4 v[102:105], v[230:237], v[214:221], v[102:105], v189, v189 op_sel_hi:[0,0,0]
	v_mfma_scale_f32_16x16x128_f8f6f4 v[98:101], v[238:245], v[214:221], v[98:101], v189, v189 op_sel_hi:[0,0,0]
	v_mfma_scale_f32_16x16x128_f8f6f4 v[86:89], v[230:237], v[222:229], v[86:89], v189, v189 op_sel_hi:[0,0,0]
	v_mfma_scale_f32_16x16x128_f8f6f4 v[82:85], v[238:245], v[222:229], v[82:85], v189, v189 op_sel_hi:[0,0,0]
	s_setprio 0
	s_mov_b32 m0, s43
	s_barrier
	ds_read_b128 v[192:195], v188 offset:49152
	ds_read_b128 v[196:199], v188 offset:50176
	ds_read_b128 v[206:209], v188 offset:51200
	ds_read_b128 v[210:213], v188 offset:52224
	ds_read_b128 v[214:217], v188 offset:53248
	ds_read_b128 v[218:221], v188 offset:54272
	ds_read_b128 v[222:225], v188 offset:55296
	ds_read_b128 v[226:229], v188 offset:56320
	global_load_lds_dwordx4 v152, s[56:57]
	s_mov_b32 m0, s44
	s_nop 0
	global_load_lds_dwordx4 v148, s[56:57]
	s_barrier
	s_waitcnt lgkmcnt(0)
	s_setprio 1
	s_waitcnt lgkmcnt(0)
	v_mfma_scale_f32_16x16x128_f8f6f4 v[78:81], v[2:9], v[192:199], v[78:81], v189, v189 op_sel_hi:[0,0,0]
	v_mfma_scale_f32_16x16x128_f8f6f4 v[74:77], v[10:17], v[192:199], v[74:77], v189, v189 op_sel_hi:[0,0,0]
	v_mfma_scale_f32_16x16x128_f8f6f4 v[62:65], v[2:9], v[206:213], v[62:65], v189, v189 op_sel_hi:[0,0,0]
	v_mfma_scale_f32_16x16x128_f8f6f4 v[58:61], v[10:17], v[206:213], v[58:61], v189, v189 op_sel_hi:[0,0,0]
	v_mfma_scale_f32_16x16x128_f8f6f4 v[46:49], v[2:9], v[214:221], v[46:49], v189, v189 op_sel_hi:[0,0,0]
	v_mfma_scale_f32_16x16x128_f8f6f4 v[42:45], v[10:17], v[214:221], v[42:45], v189, v189 op_sel_hi:[0,0,0]
	v_mfma_scale_f32_16x16x128_f8f6f4 v[30:33], v[2:9], v[222:229], v[30:33], v189, v189 op_sel_hi:[0,0,0]
	v_mfma_scale_f32_16x16x128_f8f6f4 v[26:29], v[10:17], v[222:229], v[26:29], v189, v189 op_sel_hi:[0,0,0]
	s_setprio 0
	s_barrier
	s_add_u32 s28, s28, 0x40080
	s_addc_u32 s29, s29, 0
	s_add_i32 s30, s30, s34
	s_mov_b32 m0, s30
	s_nop 0
	global_load_lds_dwordx4 v150, s[28:29]
	s_add_i32 m0, s30, 0x2000
	s_nop 0
	global_load_lds_dwordx4 v146, s[28:29]
	s_waitcnt vmcnt(6)
	s_barrier
	s_setprio 1
	v_mfma_scale_f32_16x16x128_f8f6f4 v[70:73], v[230:237], v[192:199], v[70:73], v189, v189 op_sel_hi:[0,0,0]
	v_mfma_scale_f32_16x16x128_f8f6f4 v[66:69], v[238:245], v[192:199], v[66:69], v189, v189 op_sel_hi:[0,0,0]
	v_mfma_scale_f32_16x16x128_f8f6f4 v[54:57], v[230:237], v[206:213], v[54:57], v189, v189 op_sel_hi:[0,0,0]
	v_mfma_scale_f32_16x16x128_f8f6f4 v[50:53], v[238:245], v[206:213], v[50:53], v189, v189 op_sel_hi:[0,0,0]
	v_mfma_scale_f32_16x16x128_f8f6f4 v[38:41], v[230:237], v[214:221], v[38:41], v189, v189 op_sel_hi:[0,0,0]
	v_mfma_scale_f32_16x16x128_f8f6f4 v[34:37], v[238:245], v[214:221], v[34:37], v189, v189 op_sel_hi:[0,0,0]
	v_mfma_scale_f32_16x16x128_f8f6f4 v[22:25], v[230:237], v[222:229], v[22:25], v189, v189 op_sel_hi:[0,0,0]
	v_mfma_scale_f32_16x16x128_f8f6f4 v[18:21], v[238:245], v[222:229], v[18:21], v189, v189 op_sel_hi:[0,0,0]
	s_setprio 0
	s_add_i32 s52, s52, 2
	s_add_u32 s26, s26, 0x100
	s_addc_u32 s27, s27, 0
	s_add_u32 s50, s50, 0x100
	s_addc_u32 s51, s51, 0
	s_cmp_gt_u32 s52, 13
	s_barrier
	s_cbranch_scc0 .LBB0_495
	s_lshl_b32 s28, s22, 8
	s_cmpk_gt_i32 s22, 0x7f
	s_mov_b64 s[30:31], -1
	s_cbranch_scc0 .LBB0_498
	s_add_i32 s6, s28, 0xffff8000
	v_readlane_b32 s60, v254, 18
	s_lshl_b64 s[26:27], s[6:7], 13
	v_readlane_b32 s64, v254, 22
	v_readlane_b32 s65, v254, 23
	s_add_u32 s26, s64, s26
	v_readlane_b32 s61, v254, 19
	v_readlane_b32 s62, v254, 20
	v_readlane_b32 s63, v254, 21
	v_readlane_b32 s66, v254, 24
	v_readlane_b32 s67, v254, 25
	v_readlane_b32 s68, v254, 26
	v_readlane_b32 s69, v254, 27
	v_readlane_b32 s70, v254, 28
	v_readlane_b32 s71, v254, 29
	v_readlane_b32 s72, v254, 30
	v_readlane_b32 s73, v254, 31
	v_readlane_b32 s74, v254, 32
	v_readlane_b32 s75, v254, 33
	s_addc_u32 s27, s65, s27
	s_mov_b32 s29, s7
	s_mov_b64 s[30:31], 0
